# chained MoE down units: the L1 invalidate after the tile-ready poll is dropped (a tile's activation rows are read once per XCD by the unit that waits; this CU only ever stored its own slice of them, w
# baseline (speedup 1.0000x reference)
.LBB0_1901:
	s_waitcnt vmcnt(0)
	s_waitcnt vmcnt(0)
